# split-K tail read-back (gate|up np=2, proj1 np=4): only the active q-groups prefetched in one batch per partner part
# speedup vs baseline: 1.0169x; 1.0169x over previous
.LBB0_1024:
	s_or_b32 s6, s6, s27
	s_ashr_i32 s7, s6, 31
	s_lshl_b64 s[42:43], s[6:7], 17
	v_lshl_add_u64 v[158:159], v[142:143], 0, s[42:43]
	v_mov_b32_e32 v250, s33
	v_lshlrev_b32_e32 v250, 16, v250
	v_add_co_u32_e32 v250, vcc, v250, v158
	s_nop 1
	v_addc_co_u32_e32 v251, vcc, 0, v159, vcc
	global_load_dwordx4 v[184:187], v[250:251], off
	global_load_dwordx4 v[188:191], v[250:251], off offset:1024
	v_add_co_u32_e32 v248, vcc, 0x4000, v250
	s_nop 1
	v_addc_co_u32_e32 v249, vcc, 0, v251, vcc
	global_load_dwordx4 v[192:195], v[248:249], off
	global_load_dwordx4 v[196:199], v[248:249], off offset:1024
	v_add_co_u32_e32 v248, vcc, 0x8000, v250
	s_nop 1
	v_addc_co_u32_e32 v249, vcc, 0, v251, vcc
	global_load_dwordx4 v[200:203], v[248:249], off
	global_load_dwordx4 v[204:207], v[248:249], off offset:1024
	v_add_co_u32_e32 v248, vcc, 0xc000, v250
	s_nop 1
	v_addc_co_u32_e32 v249, vcc, 0, v251, vcc
	global_load_dwordx4 v[208:211], v[248:249], off
	global_load_dwordx4 v[212:215], v[248:249], off offset:1024
	v_cndmask_b32_e64 v138, 0, 1, s[36:37]
	v_cmp_ne_u32_e64 s[6:7], 1, v138
	s_andn2_b64 vcc, exec, s[36:37]
	v_lshl_add_u64 v[158:159], v[142:143], 0, s[42:43]
	s_cbranch_vccz .LBB0_1032
	s_and_b64 vcc, exec, s[6:7]
	s_cbranch_vccz .LBB0_1033

.LBB0_1029:
	s_waitcnt vmcnt(0)
	v_lshlrev_b32_e32 v178, 16, v184
	v_and_b32_e32 v179, 0xffff0000, v184
	v_lshlrev_b32_e32 v184, 16, v185
	v_and_b32_e32 v185, 0xffff0000, v185
	v_lshlrev_b32_e32 v180, 16, v186
	v_and_b32_e32 v181, 0xffff0000, v186
	v_lshlrev_b32_e32 v186, 16, v187
	v_and_b32_e32 v187, 0xffff0000, v187
	v_pk_add_f32 v[62:63], v[62:63], v[184:185]
	v_pk_add_f32 v[54:55], v[54:55], v[186:187]
	v_pk_add_f32 v[60:61], v[60:61], v[178:179]
	v_pk_add_f32 v[52:53], v[52:53], v[180:181]
	s_waitcnt vmcnt(0)
	v_lshlrev_b32_e32 v176, 16, v188
	v_and_b32_e32 v177, 0xffff0000, v188
	v_lshlrev_b32_e32 v188, 16, v189
	v_and_b32_e32 v189, 0xffff0000, v189
	v_lshlrev_b32_e32 v178, 16, v190
	v_and_b32_e32 v179, 0xffff0000, v190
	v_lshlrev_b32_e32 v190, 16, v191
	v_and_b32_e32 v191, 0xffff0000, v191
	v_pk_add_f32 v[58:59], v[58:59], v[188:189]
	v_pk_add_f32 v[56:57], v[56:57], v[176:177]
	v_pk_add_f32 v[50:51], v[50:51], v[190:191]
	v_pk_add_f32 v[48:49], v[48:49], v[178:179]
	s_and_b64 vcc, exec, s[6:7]
	s_cbranch_vccz .LBB0_1037

.LBB0_1031:
	s_waitcnt vmcnt(0)
	v_lshlrev_b32_e32 v178, 16, v200
	v_and_b32_e32 v179, 0xffff0000, v200
	v_lshlrev_b32_e32 v200, 16, v201
	v_and_b32_e32 v201, 0xffff0000, v201
	v_lshlrev_b32_e32 v180, 16, v202
	v_and_b32_e32 v181, 0xffff0000, v202
	v_lshlrev_b32_e32 v202, 16, v203
	v_and_b32_e32 v203, 0xffff0000, v203
	v_pk_add_f32 v[30:31], v[30:31], v[200:201]
	v_pk_add_f32 v[22:23], v[22:23], v[202:203]
	v_pk_add_f32 v[28:29], v[28:29], v[178:179]
	v_pk_add_f32 v[20:21], v[20:21], v[180:181]
	s_waitcnt vmcnt(0)
	v_lshlrev_b32_e32 v176, 16, v204
	v_and_b32_e32 v177, 0xffff0000, v204
	v_lshlrev_b32_e32 v204, 16, v205
	v_and_b32_e32 v205, 0xffff0000, v205
	v_lshlrev_b32_e32 v178, 16, v206
	v_and_b32_e32 v179, 0xffff0000, v206
	v_lshlrev_b32_e32 v206, 16, v207
	v_and_b32_e32 v207, 0xffff0000, v207
	v_pk_add_f32 v[26:27], v[26:27], v[204:205]
	v_pk_add_f32 v[24:25], v[24:25], v[176:177]
	v_pk_add_f32 v[18:19], v[18:19], v[206:207]
	v_pk_add_f32 v[16:17], v[16:17], v[178:179]
	s_and_b64 vcc, exec, s[6:7]
	s_cbranch_vccz .LBB0_1039
	s_branch .LBB0_1040

.LBB0_1037:
	s_waitcnt vmcnt(0)
	v_lshlrev_b32_e32 v178, 16, v192
	v_and_b32_e32 v179, 0xffff0000, v192
	v_lshlrev_b32_e32 v192, 16, v193
	v_and_b32_e32 v193, 0xffff0000, v193
	v_lshlrev_b32_e32 v180, 16, v194
	v_and_b32_e32 v181, 0xffff0000, v194
	v_lshlrev_b32_e32 v194, 16, v195
	v_and_b32_e32 v195, 0xffff0000, v195
	v_pk_add_f32 v[46:47], v[46:47], v[192:193]
	v_pk_add_f32 v[38:39], v[38:39], v[194:195]
	v_pk_add_f32 v[44:45], v[44:45], v[178:179]
	v_pk_add_f32 v[36:37], v[36:37], v[180:181]
	s_waitcnt vmcnt(0)
	v_lshlrev_b32_e32 v176, 16, v196
	v_and_b32_e32 v177, 0xffff0000, v196
	v_lshlrev_b32_e32 v196, 16, v197
	v_and_b32_e32 v197, 0xffff0000, v197
	v_lshlrev_b32_e32 v178, 16, v198
	v_and_b32_e32 v179, 0xffff0000, v198
	v_lshlrev_b32_e32 v198, 16, v199
	v_and_b32_e32 v199, 0xffff0000, v199
	v_pk_add_f32 v[42:43], v[42:43], v[196:197]
	v_pk_add_f32 v[40:41], v[40:41], v[176:177]
	v_pk_add_f32 v[34:35], v[34:35], v[198:199]
	v_pk_add_f32 v[32:33], v[32:33], v[178:179]
	s_and_b64 vcc, exec, s[6:7]
	s_cbranch_vccz .LBB0_1031

.LBB0_1039:
	s_waitcnt vmcnt(0)
	v_lshlrev_b32_e32 v176, 16, v208
	v_and_b32_e32 v177, 0xffff0000, v208
	v_lshlrev_b32_e32 v208, 16, v209
	v_and_b32_e32 v209, 0xffff0000, v209
	v_lshlrev_b32_e32 v178, 16, v210
	v_and_b32_e32 v179, 0xffff0000, v210
	v_lshlrev_b32_e32 v210, 16, v211
	v_and_b32_e32 v211, 0xffff0000, v211
	v_pk_add_f32 v[14:15], v[14:15], v[208:209]
	v_pk_add_f32 v[6:7], v[6:7], v[210:211]
	v_pk_add_f32 v[12:13], v[12:13], v[176:177]
	v_pk_add_f32 v[4:5], v[4:5], v[178:179]
	s_waitcnt vmcnt(0)
	v_lshlrev_b32_e32 v158, 16, v212
	v_and_b32_e32 v159, 0xffff0000, v212
	v_lshlrev_b32_e32 v212, 16, v213
	v_and_b32_e32 v213, 0xffff0000, v213
	v_lshlrev_b32_e32 v176, 16, v214
	v_and_b32_e32 v177, 0xffff0000, v214
	v_lshlrev_b32_e32 v214, 16, v215
	v_and_b32_e32 v215, 0xffff0000, v215
	v_pk_add_f32 v[10:11], v[10:11], v[212:213]
	v_pk_add_f32 v[8:9], v[8:9], v[158:159]
	v_pk_add_f32 v[2:3], v[2:3], v[214:215]
	v_pk_add_f32 v[0:1], v[0:1], v[176:177]

.LBB0_1291:
	v_subrev_co_u32_e32 v136, vcc, 1, v136
	s_and_b64 vcc, exec, vcc
	s_cbranch_vccnz .LBB0_1290
	s_ashr_i32 s29, s28, 31
	s_lshl_b64 s[48:49], s[28:29], 17
	v_lshl_add_u64 v[148:149], v[138:139], 0, s[48:49]
	v_mov_b32_e32 v250, s35
	v_lshlrev_b32_e32 v250, 15, v250
	v_add_co_u32_e32 v250, vcc, v250, v148
	s_nop 1
	v_addc_co_u32_e32 v251, vcc, 0, v149, vcc
	global_load_dwordx4 v[184:187], v[250:251], off
	global_load_dwordx4 v[188:191], v[250:251], off offset:1024
	v_add_co_u32_e32 v248, vcc, 0x4000, v250
	s_nop 1
	v_addc_co_u32_e32 v249, vcc, 0, v251, vcc
	global_load_dwordx4 v[192:195], v[248:249], off
	global_load_dwordx4 v[196:199], v[248:249], off offset:1024
	s_andn2_b64 vcc, exec, s[30:31]
	s_cbranch_vccnz .LBB0_1300
	s_waitcnt vmcnt(0)
	v_lshlrev_b32_e32 v162, 16, v184
	v_and_b32_e32 v163, 0xffff0000, v184
	v_lshlrev_b32_e32 v184, 16, v185
	v_and_b32_e32 v185, 0xffff0000, v185
	v_lshlrev_b32_e32 v164, 16, v186
	v_and_b32_e32 v165, 0xffff0000, v186
	v_lshlrev_b32_e32 v186, 16, v187
	v_and_b32_e32 v187, 0xffff0000, v187
	v_pk_add_f32 v[126:127], v[126:127], v[184:185]
	v_pk_add_f32 v[122:123], v[122:123], v[186:187]
	v_pk_add_f32 v[124:125], v[124:125], v[162:163]
	v_pk_add_f32 v[120:121], v[120:121], v[164:165]
	s_waitcnt vmcnt(0)
	v_lshlrev_b32_e32 v162, 16, v188
	v_and_b32_e32 v163, 0xffff0000, v188
	v_lshlrev_b32_e32 v188, 16, v189
	v_and_b32_e32 v189, 0xffff0000, v189
	v_lshlrev_b32_e32 v164, 16, v190
	v_and_b32_e32 v165, 0xffff0000, v190
	v_lshlrev_b32_e32 v190, 16, v191
	v_and_b32_e32 v191, 0xffff0000, v191
	v_pk_add_f32 v[114:115], v[114:115], v[188:189]
	v_pk_add_f32 v[112:113], v[112:113], v[162:163]
	v_pk_add_f32 v[106:107], v[106:107], v[190:191]
	v_pk_add_f32 v[104:105], v[104:105], v[164:165]
	s_andn2_b64 vcc, exec, s[36:37]
	s_cbranch_vccz .LBB0_1301

.LBB0_1295:
	s_waitcnt vmcnt(0)
	v_lshlrev_b32_e32 v164, 16, v184
	v_and_b32_e32 v165, 0xffff0000, v184
	v_lshlrev_b32_e32 v184, 16, v185
	v_and_b32_e32 v185, 0xffff0000, v185
	v_lshlrev_b32_e32 v166, 16, v186
	v_and_b32_e32 v167, 0xffff0000, v186
	v_lshlrev_b32_e32 v186, 16, v187
	v_and_b32_e32 v187, 0xffff0000, v187
	v_pk_add_f32 v[102:103], v[102:103], v[184:185]
	v_pk_add_f32 v[94:95], v[94:95], v[186:187]
	v_pk_add_f32 v[100:101], v[100:101], v[164:165]
	v_pk_add_f32 v[92:93], v[92:93], v[166:167]
	s_waitcnt vmcnt(0)
	v_lshlrev_b32_e32 v162, 16, v188
	v_and_b32_e32 v163, 0xffff0000, v188
	v_lshlrev_b32_e32 v188, 16, v189
	v_and_b32_e32 v189, 0xffff0000, v189
	v_lshlrev_b32_e32 v164, 16, v190
	v_and_b32_e32 v165, 0xffff0000, v190
	v_lshlrev_b32_e32 v190, 16, v191
	v_and_b32_e32 v191, 0xffff0000, v191
	v_pk_add_f32 v[82:83], v[82:83], v[188:189]
	v_pk_add_f32 v[80:81], v[80:81], v[162:163]
	v_pk_add_f32 v[74:75], v[74:75], v[190:191]
	v_pk_add_f32 v[72:73], v[72:73], v[164:165]
	s_andn2_b64 vcc, exec, s[40:41]
	s_cbranch_vccz .LBB0_1303

.LBB0_1297:
	s_waitcnt vmcnt(0)
	v_lshlrev_b32_e32 v164, 16, v184
	v_and_b32_e32 v165, 0xffff0000, v184
	v_lshlrev_b32_e32 v184, 16, v185
	v_and_b32_e32 v185, 0xffff0000, v185
	v_lshlrev_b32_e32 v166, 16, v186
	v_and_b32_e32 v167, 0xffff0000, v186
	v_lshlrev_b32_e32 v186, 16, v187
	v_and_b32_e32 v187, 0xffff0000, v187
	v_pk_add_f32 v[62:63], v[62:63], v[184:185]
	v_pk_add_f32 v[58:59], v[58:59], v[186:187]
	v_pk_add_f32 v[60:61], v[60:61], v[164:165]
	v_pk_add_f32 v[56:57], v[56:57], v[166:167]
	s_waitcnt vmcnt(0)
	v_lshlrev_b32_e32 v162, 16, v188
	v_and_b32_e32 v163, 0xffff0000, v188
	v_lshlrev_b32_e32 v188, 16, v189
	v_and_b32_e32 v189, 0xffff0000, v189
	v_lshlrev_b32_e32 v164, 16, v190
	v_and_b32_e32 v165, 0xffff0000, v190
	v_lshlrev_b32_e32 v190, 16, v191
	v_and_b32_e32 v191, 0xffff0000, v191
	v_pk_add_f32 v[50:51], v[50:51], v[188:189]
	v_pk_add_f32 v[48:49], v[48:49], v[162:163]
	v_pk_add_f32 v[42:43], v[42:43], v[190:191]
	v_pk_add_f32 v[40:41], v[40:41], v[164:165]
	s_andn2_b64 vcc, exec, s[44:45]
	s_cbranch_vccz .LBB0_1305

.LBB0_1299:
	s_waitcnt vmcnt(0)
	v_lshlrev_b32_e32 v164, 16, v184
	v_and_b32_e32 v165, 0xffff0000, v184
	v_lshlrev_b32_e32 v184, 16, v185
	v_and_b32_e32 v185, 0xffff0000, v185
	v_lshlrev_b32_e32 v166, 16, v186
	v_and_b32_e32 v167, 0xffff0000, v186
	v_lshlrev_b32_e32 v186, 16, v187
	v_and_b32_e32 v187, 0xffff0000, v187
	v_pk_add_f32 v[38:39], v[38:39], v[184:185]
	v_pk_add_f32 v[30:31], v[30:31], v[186:187]
	v_pk_add_f32 v[36:37], v[36:37], v[164:165]
	v_pk_add_f32 v[28:29], v[28:29], v[166:167]
	s_waitcnt vmcnt(0)
	v_lshlrev_b32_e32 v162, 16, v188
	v_and_b32_e32 v163, 0xffff0000, v188
	v_lshlrev_b32_e32 v188, 16, v189
	v_and_b32_e32 v189, 0xffff0000, v189
	v_lshlrev_b32_e32 v164, 16, v190
	v_and_b32_e32 v165, 0xffff0000, v190
	v_lshlrev_b32_e32 v190, 16, v191
	v_and_b32_e32 v191, 0xffff0000, v191
	v_pk_add_f32 v[18:19], v[18:19], v[188:189]
	v_pk_add_f32 v[16:17], v[16:17], v[162:163]
	v_pk_add_f32 v[10:11], v[10:11], v[190:191]
	v_pk_add_f32 v[8:9], v[8:9], v[164:165]
	s_andn2_b64 vcc, exec, s[62:63]
	s_cbranch_vccnz .LBB0_1290
	s_branch .LBB0_1307

.LBB0_1303:
	s_waitcnt vmcnt(0)
	v_lshlrev_b32_e32 v164, 16, v192
	v_and_b32_e32 v165, 0xffff0000, v192
	v_lshlrev_b32_e32 v192, 16, v193
	v_and_b32_e32 v193, 0xffff0000, v193
	v_lshlrev_b32_e32 v166, 16, v194
	v_and_b32_e32 v167, 0xffff0000, v194
	v_lshlrev_b32_e32 v194, 16, v195
	v_and_b32_e32 v195, 0xffff0000, v195
	v_pk_add_f32 v[86:87], v[86:87], v[192:193]
	v_pk_add_f32 v[78:79], v[78:79], v[194:195]
	v_pk_add_f32 v[84:85], v[84:85], v[164:165]
	v_pk_add_f32 v[76:77], v[76:77], v[166:167]
	s_waitcnt vmcnt(0)
	v_lshlrev_b32_e32 v162, 16, v196
	v_and_b32_e32 v163, 0xffff0000, v196
	v_lshlrev_b32_e32 v196, 16, v197
	v_and_b32_e32 v197, 0xffff0000, v197
	v_lshlrev_b32_e32 v164, 16, v198
	v_and_b32_e32 v165, 0xffff0000, v198
	v_lshlrev_b32_e32 v198, 16, v199
	v_and_b32_e32 v199, 0xffff0000, v199
	v_pk_add_f32 v[70:71], v[70:71], v[196:197]
	v_pk_add_f32 v[68:69], v[68:69], v[162:163]
	v_pk_add_f32 v[66:67], v[66:67], v[198:199]
	v_pk_add_f32 v[64:65], v[64:65], v[164:165]
	s_andn2_b64 vcc, exec, s[42:43]
	s_cbranch_vccz .LBB0_1297

.LBB0_1305:
	s_waitcnt vmcnt(0)
	v_lshlrev_b32_e32 v164, 16, v192
	v_and_b32_e32 v165, 0xffff0000, v192
	v_lshlrev_b32_e32 v192, 16, v193
	v_and_b32_e32 v193, 0xffff0000, v193
	v_lshlrev_b32_e32 v166, 16, v194
	v_and_b32_e32 v167, 0xffff0000, v194
	v_lshlrev_b32_e32 v194, 16, v195
	v_and_b32_e32 v195, 0xffff0000, v195
	v_pk_add_f32 v[54:55], v[54:55], v[192:193]
	v_pk_add_f32 v[46:47], v[46:47], v[194:195]
	v_pk_add_f32 v[52:53], v[52:53], v[164:165]
	v_pk_add_f32 v[44:45], v[44:45], v[166:167]
	s_waitcnt vmcnt(0)
	v_lshlrev_b32_e32 v162, 16, v196
	v_and_b32_e32 v163, 0xffff0000, v196
	v_lshlrev_b32_e32 v196, 16, v197
	v_and_b32_e32 v197, 0xffff0000, v197
	v_lshlrev_b32_e32 v164, 16, v198
	v_and_b32_e32 v165, 0xffff0000, v198
	v_lshlrev_b32_e32 v198, 16, v199
	v_and_b32_e32 v199, 0xffff0000, v199
	v_pk_add_f32 v[34:35], v[34:35], v[196:197]
	v_pk_add_f32 v[32:33], v[32:33], v[162:163]
	v_pk_add_f32 v[26:27], v[26:27], v[198:199]
	v_pk_add_f32 v[24:25], v[24:25], v[164:165]
	s_andn2_b64 vcc, exec, s[46:47]
	s_cbranch_vccz .LBB0_1299

.LBB0_1307:
	s_waitcnt vmcnt(0)
	v_lshlrev_b32_e32 v162, 16, v192
	v_and_b32_e32 v163, 0xffff0000, v192
	v_lshlrev_b32_e32 v192, 16, v193
	v_and_b32_e32 v193, 0xffff0000, v193
	v_lshlrev_b32_e32 v164, 16, v194
	v_and_b32_e32 v165, 0xffff0000, v194
	v_lshlrev_b32_e32 v194, 16, v195
	v_and_b32_e32 v195, 0xffff0000, v195
	v_pk_add_f32 v[22:23], v[22:23], v[192:193]
	v_pk_add_f32 v[14:15], v[14:15], v[194:195]
	v_pk_add_f32 v[20:21], v[20:21], v[162:163]
	v_pk_add_f32 v[12:13], v[12:13], v[164:165]
	s_waitcnt vmcnt(0)
	v_lshlrev_b32_e32 v148, 16, v196
	v_and_b32_e32 v149, 0xffff0000, v196
	v_lshlrev_b32_e32 v196, 16, v197
	v_and_b32_e32 v197, 0xffff0000, v197
	v_lshlrev_b32_e32 v162, 16, v198
	v_and_b32_e32 v163, 0xffff0000, v198
	v_lshlrev_b32_e32 v198, 16, v199
	v_and_b32_e32 v199, 0xffff0000, v199
	v_pk_add_f32 v[6:7], v[6:7], v[196:197]
	v_pk_add_f32 v[4:5], v[4:5], v[148:149]
	v_pk_add_f32 v[2:3], v[2:3], v[198:199]
	v_pk_add_f32 v[0:1], v[0:1], v[162:163]
	s_branch .LBB0_1290
